# NA unit prologue (tile 0 staging): 16-lane sums of squares via DPP adds instead of ds_bpermute round trips; on top of v71
# speedup vs baseline: 1.0031x; 1.0031x over previous
.LBB0_468:
	s_or_b64 exec, exec, s[4:5]
	s_ashr_i32 s94, s0, 9
	v_readlane_b32 s0, v252, 17
	s_add_i32 s92, s95, -4
	s_lshl_b32 s1, s86, 13
	v_or_b32_e32 v12, s0, v0
	v_readlane_b32 s0, v252, 24
	s_add_i32 s85, s86, s0
	s_lshl_b32 s0, s94, 3
	s_or_b32 s2, s0, s75
	s_ashr_i32 s3, s2, 31
	s_lshl_b32 s0, s86, 6
	s_lshl_b64 s[72:73], s[2:3], 21
	v_readlane_b32 s2, v252, 18
	s_add_u32 s2, s2, s72
	v_readlane_b32 s3, v252, 19
	s_addc_u32 s3, s3, s73
	s_add_u32 s2, s2, s1
	s_addc_u32 s3, s3, 0
	s_lshl_b64 s[96:97], s[92:93], 13
	s_add_u32 s1, s96, s72
	s_addc_u32 s4, s97, s73
	v_readlane_b32 s5, v252, 20
	s_add_u32 s6, s5, s1
	v_readlane_b32 s5, v252, 21
	s_addc_u32 s7, s5, s4
	v_readlane_b32 s5, v252, 22
	s_add_u32 s8, s5, s1
	v_readlane_b32 s1, v252, 23
	s_addc_u32 s9, s1, s4
	s_mov_b64 s[4:5], s[64:65]
	s_load_dwordx2 s[12:13], s[4:5], 0x28
	s_load_dwordx2 s[10:11], s[64:65], 0x30
	v_mbcnt_lo_u32_b32 v16, -1, 0
	v_mbcnt_hi_u32_b32 v16, -1, v16
	v_readlane_b32 s4, v252, 13
	v_and_b32_e32 v176, 31, v16
	v_ashrrev_i32_e32 v177, 5, v16
	v_or_b32_e32 v0, s4, v176
	v_lshlrev_b64 v[2:3], 7, v[0:1]
	v_lshl_add_u64 v[4:5], s[2:3], 0, v[2:3]
	v_lshlrev_b32_e32 v2, 3, v177
	v_ashrrev_i32_e32 v3, 31, v2
	v_lshl_add_u64 v[4:5], v[4:5], 0, v[2:3]
	global_load_dwordx2 v[6:7], v[4:5], off
	v_readlane_b32 s5, v252, 14
	v_readlane_b32 s1, v252, 11
	v_med3_u32 v15, v12, 8, 56
	v_add_u32_e32 v14, -8, v15
	v_lshlrev_b32_e32 v178, 4, v177
	s_mov_b32 s3, 0
	v_lshlrev_b32_e32 v189, 8, v176
	v_lshl_add_u32 v179, v176, 2, s89
	v_mov_b32_e32 v200, 0
	v_mov_b32_e32 v184, 0xf149f2ca
	s_waitcnt vmcnt(0)
	v_cvt_f32_fp8_e32 v0, v6
	v_cvt_f32_fp8_sdwa v8, v6 src0_sel:BYTE_1
	v_cvt_pk_bf16_f32 v0, v0, v8
	v_cvt_f32_fp8_sdwa v8, v6 src0_sel:BYTE_2
	v_cvt_f32_fp8_sdwa v6, v6 src0_sel:BYTE_3
	v_cvt_pk_bf16_f32 v8, v8, v6
	v_cvt_f32_fp8_e32 v6, v7
	v_cvt_f32_fp8_sdwa v9, v7 src0_sel:BYTE_1
	v_cvt_pk_bf16_f32 v9, v6, v9
	v_cvt_f32_fp8_sdwa v6, v7 src0_sel:BYTE_2
	v_cvt_f32_fp8_sdwa v7, v7 src0_sel:BYTE_3
	v_cvt_pk_bf16_f32 v10, v6, v7
	global_load_dwordx2 v[6:7], v[4:5], off offset:16
	v_and_b32_e32 v80, 0xffff0000, v0
	v_and_b32_e32 v78, 0xffff0000, v8
	v_lshlrev_b32_e32 v81, 16, v0
	v_lshlrev_b32_e32 v79, 16, v8
	v_mul_f32_e32 v0, v80, v80
	v_mul_f32_e32 v8, v78, v78
	v_and_b32_e32 v76, 0xffff0000, v9
	v_fmac_f32_e32 v0, v81, v81
	v_fmac_f32_e32 v8, v79, v79
	v_lshlrev_b32_e32 v77, 16, v9
	v_add_f32_e32 v0, v0, v8
	v_mul_f32_e32 v8, v76, v76
	v_and_b32_e32 v74, 0xffff0000, v10
	v_fmac_f32_e32 v8, v77, v77
	v_lshlrev_b32_e32 v75, 16, v10
	v_add_f32_e32 v0, v0, v8
	v_mul_f32_e32 v8, v74, v74
	v_fmac_f32_e32 v8, v75, v75
	v_add_f32_e32 v0, v0, v8
	s_waitcnt vmcnt(0)
	v_cvt_f32_fp8_e32 v11, v6
	v_cvt_f32_fp8_sdwa v17, v6 src0_sel:BYTE_1
	v_cvt_pk_bf16_f32 v11, v11, v17
	v_cvt_f32_fp8_sdwa v17, v6 src0_sel:BYTE_2
	v_cvt_f32_fp8_sdwa v6, v6 src0_sel:BYTE_3
	v_cvt_pk_bf16_f32 v18, v17, v6
	v_cvt_f32_fp8_e32 v6, v7
	v_cvt_f32_fp8_sdwa v17, v7 src0_sel:BYTE_1
	v_cvt_pk_bf16_f32 v19, v6, v17
	v_cvt_f32_fp8_sdwa v6, v7 src0_sel:BYTE_2
	v_cvt_f32_fp8_sdwa v7, v7 src0_sel:BYTE_3
	v_cvt_pk_bf16_f32 v20, v6, v7
	global_load_dwordx2 v[6:7], v[4:5], off offset:32
	v_and_b32_e32 v72, 0xffff0000, v11
	v_and_b32_e32 v70, 0xffff0000, v18
	v_lshlrev_b32_e32 v73, 16, v11
	v_lshlrev_b32_e32 v71, 16, v18
	v_mul_f32_e32 v8, v72, v72
	v_mul_f32_e32 v9, v70, v70
	v_and_b32_e32 v68, 0xffff0000, v19
	v_fmac_f32_e32 v8, v73, v73
	v_fmac_f32_e32 v9, v71, v71
	v_lshlrev_b32_e32 v69, 16, v19
	v_add_f32_e32 v8, v8, v9
	v_mul_f32_e32 v9, v68, v68
	v_and_b32_e32 v66, 0xffff0000, v20
	v_fmac_f32_e32 v9, v69, v69
	v_lshlrev_b32_e32 v67, 16, v20
	v_add_f32_e32 v8, v8, v9
	v_mul_f32_e32 v9, v66, v66
	v_fmac_f32_e32 v9, v67, v67
	v_add_f32_e32 v8, v8, v9
	v_add_f32_e32 v0, v0, v8
	s_waitcnt lgkmcnt(0)
	v_lshl_add_u64 v[10:11], v[2:3], 2, s[12:13]
	s_waitcnt vmcnt(0)
	v_cvt_f32_fp8_e32 v17, v6
	v_cvt_f32_fp8_sdwa v21, v6 src0_sel:BYTE_1
	v_cvt_pk_bf16_f32 v21, v17, v21
	v_cvt_f32_fp8_sdwa v17, v6 src0_sel:BYTE_2
	v_cvt_f32_fp8_sdwa v6, v6 src0_sel:BYTE_3
	v_cvt_pk_bf16_f32 v22, v17, v6
	v_cvt_f32_fp8_e32 v6, v7
	v_cvt_f32_fp8_sdwa v17, v7 src0_sel:BYTE_1
	v_cvt_pk_bf16_f32 v23, v6, v17
	v_cvt_f32_fp8_sdwa v6, v7 src0_sel:BYTE_2
	v_cvt_f32_fp8_sdwa v7, v7 src0_sel:BYTE_3
	v_cvt_pk_bf16_f32 v24, v6, v7
	global_load_dwordx2 v[6:7], v[4:5], off offset:48
	v_and_b32_e32 v64, 0xffff0000, v21
	v_and_b32_e32 v62, 0xffff0000, v22
	v_lshlrev_b32_e32 v65, 16, v21
	v_lshlrev_b32_e32 v63, 16, v22
	v_mul_f32_e32 v8, v64, v64
	v_mul_f32_e32 v9, v62, v62
	v_and_b32_e32 v60, 0xffff0000, v23
	v_fmac_f32_e32 v8, v65, v65
	v_fmac_f32_e32 v9, v63, v63
	v_lshlrev_b32_e32 v61, 16, v23
	v_add_f32_e32 v8, v8, v9
	v_mul_f32_e32 v9, v60, v60
	v_and_b32_e32 v58, 0xffff0000, v24
	v_fmac_f32_e32 v9, v61, v61
	v_lshlrev_b32_e32 v59, 16, v24
	v_add_f32_e32 v8, v8, v9
	v_mul_f32_e32 v9, v58, v58
	v_fmac_f32_e32 v9, v59, v59
	v_add_f32_e32 v8, v8, v9
	v_add_f32_e32 v0, v0, v8
	s_waitcnt vmcnt(0)
	v_cvt_f32_fp8_e32 v17, v6
	v_cvt_f32_fp8_sdwa v25, v6 src0_sel:BYTE_1
	v_cvt_pk_bf16_f32 v25, v17, v25
	v_cvt_f32_fp8_sdwa v17, v6 src0_sel:BYTE_2
	v_cvt_f32_fp8_sdwa v6, v6 src0_sel:BYTE_3
	v_cvt_pk_bf16_f32 v26, v17, v6
	v_cvt_f32_fp8_e32 v6, v7
	v_cvt_f32_fp8_sdwa v17, v7 src0_sel:BYTE_1
	v_cvt_pk_bf16_f32 v27, v6, v17
	v_cvt_f32_fp8_sdwa v6, v7 src0_sel:BYTE_2
	v_cvt_f32_fp8_sdwa v7, v7 src0_sel:BYTE_3
	v_cvt_pk_bf16_f32 v28, v6, v7
	global_load_dwordx2 v[6:7], v[4:5], off offset:64
	v_and_b32_e32 v56, 0xffff0000, v25
	v_and_b32_e32 v54, 0xffff0000, v26
	v_lshlrev_b32_e32 v57, 16, v25
	v_lshlrev_b32_e32 v55, 16, v26
	v_mul_f32_e32 v8, v56, v56
	v_mul_f32_e32 v9, v54, v54
	v_and_b32_e32 v52, 0xffff0000, v27
	v_fmac_f32_e32 v8, v57, v57
	v_fmac_f32_e32 v9, v55, v55
	v_lshlrev_b32_e32 v53, 16, v27
	v_add_f32_e32 v8, v8, v9
	v_mul_f32_e32 v9, v52, v52
	v_and_b32_e32 v50, 0xffff0000, v28
	v_fmac_f32_e32 v9, v53, v53
	v_lshlrev_b32_e32 v51, 16, v28
	v_add_f32_e32 v8, v8, v9
	v_mul_f32_e32 v9, v50, v50
	v_fmac_f32_e32 v9, v51, v51
	v_add_f32_e32 v8, v8, v9
	v_add_f32_e32 v0, v0, v8
	s_waitcnt vmcnt(0)
	v_cvt_f32_fp8_e32 v17, v6
	v_cvt_f32_fp8_sdwa v29, v6 src0_sel:BYTE_1
	v_cvt_pk_bf16_f32 v29, v17, v29
	v_cvt_f32_fp8_sdwa v17, v6 src0_sel:BYTE_2
	v_cvt_f32_fp8_sdwa v6, v6 src0_sel:BYTE_3
	v_cvt_pk_bf16_f32 v30, v17, v6
	v_cvt_f32_fp8_e32 v6, v7
	v_cvt_f32_fp8_sdwa v17, v7 src0_sel:BYTE_1
	v_cvt_pk_bf16_f32 v31, v6, v17
	v_cvt_f32_fp8_sdwa v6, v7 src0_sel:BYTE_2
	v_cvt_f32_fp8_sdwa v7, v7 src0_sel:BYTE_3
	v_cvt_pk_bf16_f32 v32, v6, v7
	global_load_dwordx2 v[6:7], v[4:5], off offset:80
	v_and_b32_e32 v48, 0xffff0000, v29
	v_and_b32_e32 v46, 0xffff0000, v30
	v_lshlrev_b32_e32 v49, 16, v29
	v_lshlrev_b32_e32 v47, 16, v30
	v_mul_f32_e32 v8, v48, v48
	v_mul_f32_e32 v9, v46, v46
	v_and_b32_e32 v44, 0xffff0000, v31
	v_fmac_f32_e32 v8, v49, v49
	v_fmac_f32_e32 v9, v47, v47
	v_lshlrev_b32_e32 v45, 16, v31
	v_add_f32_e32 v8, v8, v9
	v_mul_f32_e32 v9, v44, v44
	v_and_b32_e32 v42, 0xffff0000, v32
	v_fmac_f32_e32 v9, v45, v45
	v_lshlrev_b32_e32 v43, 16, v32
	v_add_f32_e32 v8, v8, v9
	v_mul_f32_e32 v9, v42, v42
	v_fmac_f32_e32 v9, v43, v43
	v_add_f32_e32 v8, v8, v9
	v_add_f32_e32 v0, v0, v8
	s_waitcnt vmcnt(0)
	v_cvt_f32_fp8_e32 v17, v6
	v_cvt_f32_fp8_sdwa v33, v6 src0_sel:BYTE_1
	v_cvt_pk_bf16_f32 v33, v17, v33
	v_cvt_f32_fp8_sdwa v17, v6 src0_sel:BYTE_2
	v_cvt_f32_fp8_sdwa v6, v6 src0_sel:BYTE_3
	v_cvt_pk_bf16_f32 v34, v17, v6
	v_cvt_f32_fp8_e32 v6, v7
	v_cvt_f32_fp8_sdwa v17, v7 src0_sel:BYTE_1
	v_cvt_pk_bf16_f32 v35, v6, v17
	v_cvt_f32_fp8_sdwa v6, v7 src0_sel:BYTE_2
	v_cvt_f32_fp8_sdwa v7, v7 src0_sel:BYTE_3
	v_cvt_pk_bf16_f32 v82, v6, v7
	global_load_dwordx2 v[6:7], v[4:5], off offset:96
	v_and_b32_e32 v40, 0xffff0000, v33
	v_and_b32_e32 v38, 0xffff0000, v34
	v_lshlrev_b32_e32 v41, 16, v33
	v_lshlrev_b32_e32 v39, 16, v34
	v_mul_f32_e32 v8, v40, v40
	v_mul_f32_e32 v9, v38, v38
	v_fmac_f32_e32 v8, v41, v41
	v_fmac_f32_e32 v9, v39, v39
	v_lshlrev_b32_e32 v37, 16, v35
	v_add_f32_e32 v8, v8, v9
	v_and_b32_e32 v34, 0xffff0000, v82
	s_waitcnt vmcnt(0)
	v_cvt_f32_fp8_e32 v17, v6
	v_cvt_f32_fp8_sdwa v36, v6 src0_sel:BYTE_1
	v_cvt_pk_bf16_f32 v83, v17, v36
	v_cvt_f32_fp8_sdwa v17, v6 src0_sel:BYTE_2
	v_cvt_f32_fp8_sdwa v6, v6 src0_sel:BYTE_3
	v_cvt_pk_bf16_f32 v6, v17, v6
	v_cvt_f32_fp8_e32 v17, v7
	v_cvt_f32_fp8_sdwa v36, v7 src0_sel:BYTE_1
	v_cvt_pk_bf16_f32 v84, v17, v36
	v_cvt_f32_fp8_sdwa v17, v7 src0_sel:BYTE_2
	v_cvt_f32_fp8_sdwa v7, v7 src0_sel:BYTE_3
	v_cvt_pk_bf16_f32 v7, v17, v7
	global_load_dwordx2 v[4:5], v[4:5], off offset:112
	v_and_b32_e32 v32, 0xffff0000, v83
	v_and_b32_e32 v30, 0xffff0000, v6
	v_lshlrev_b32_e32 v33, 16, v83
	v_lshlrev_b32_e32 v31, 16, v6
	v_lshlrev_b32_e32 v27, 16, v7
	v_and_b32_e32 v26, 0xffff0000, v7
	v_mul_f32_e32 v6, v32, v32
	v_mul_f32_e32 v7, v30, v30
	v_and_b32_e32 v28, 0xffff0000, v84
	v_fmac_f32_e32 v6, v33, v33
	v_fmac_f32_e32 v7, v31, v31
	v_lshlrev_b32_e32 v29, 16, v84
	v_add_f32_e32 v6, v6, v7
	v_mul_f32_e32 v7, v28, v28
	v_fmac_f32_e32 v7, v29, v29
	v_add_f32_e32 v6, v6, v7
	v_mul_f32_e32 v7, v26, v26
	v_fmac_f32_e32 v7, v27, v27
	v_add_f32_e32 v6, v6, v7
	s_waitcnt vmcnt(0)
	v_cvt_f32_fp8_e32 v17, v4
	v_cvt_f32_fp8_sdwa v36, v4 src0_sel:BYTE_1
	v_cvt_pk_bf16_f32 v85, v17, v36
	v_cvt_f32_fp8_sdwa v17, v4 src0_sel:BYTE_2
	v_cvt_f32_fp8_sdwa v4, v4 src0_sel:BYTE_3
	v_cvt_f32_fp8_sdwa v36, v5 src0_sel:BYTE_1
	v_cvt_pk_bf16_f32 v4, v17, v4
	v_cvt_f32_fp8_e32 v17, v5
	v_cvt_pk_bf16_f32 v86, v17, v36
	v_and_b32_e32 v36, 0xffff0000, v35
	v_mul_f32_e32 v9, v36, v36
	v_fmac_f32_e32 v9, v37, v37
	v_lshlrev_b32_e32 v35, 16, v82
	v_add_f32_e32 v8, v8, v9
	v_mul_f32_e32 v9, v34, v34
	v_fmac_f32_e32 v9, v35, v35
	v_cvt_f32_fp8_sdwa v17, v5 src0_sel:BYTE_2
	v_cvt_f32_fp8_sdwa v5, v5 src0_sel:BYTE_3
	v_add_f32_e32 v8, v8, v9
	v_cvt_pk_bf16_f32 v5, v17, v5
	v_add_f32_e32 v0, v0, v8
	v_and_b32_e32 v23, 0xffff0000, v85
	v_and_b32_e32 v21, 0xffff0000, v4
	v_add_f32_e32 v6, v0, v6
	v_lshlrev_b32_e32 v24, 16, v85
	v_lshlrev_b32_e32 v22, 16, v4
	v_lshlrev_b32_e32 v18, 16, v5
	v_and_b32_e32 v0, 0xffff0000, v5
	v_mul_f32_e32 v4, v23, v23
	v_mul_f32_e32 v5, v21, v21
	v_and_b32_e32 v19, 0xffff0000, v86
	v_fmac_f32_e32 v4, v24, v24
	v_fmac_f32_e32 v5, v22, v22
	v_lshlrev_b32_e32 v20, 16, v86
	v_add_f32_e32 v4, v4, v5
	v_mul_f32_e32 v5, v19, v19
	v_fmac_f32_e32 v5, v20, v20
	v_add_f32_e32 v4, v4, v5
	v_mul_f32_e32 v5, v0, v0
	v_fmac_f32_e32 v5, v18, v18
	v_add_f32_e32 v4, v4, v5
	v_add_f32_e32 v4, v6, v4
	v_mov_b32_e32 v5, v4
	s_nop 1
	v_permlane32_swap_b32_e32 v4, v5
	v_add_f32_e32 v4, v4, v5
	v_fmamk_f32 v4, v4, 0x3c000000, v167
	v_rsq_f32_e32 v25, v4
	s_nop 0
	v_add_u32_e32 v17, s1, v16
	s_movk_i32 s1, 0xffef
	global_load_dwordx4 v[2:5], v[10:11], off offset:16
	global_load_dwordx4 v[6:9], v[10:11], off
	v_mul_f32_e32 v81, v25, v81
	v_mul_f32_e32 v80, v25, v80
	v_mul_f32_e32 v73, v25, v73
	v_mul_f32_e32 v72, v25, v72
	v_mul_f32_e32 v65, v25, v65
	v_mul_f32_e32 v64, v25, v64
	v_mul_f32_e32 v57, v25, v57
	v_mul_f32_e32 v56, v25, v56
	v_mul_f32_e32 v49, v25, v49
	v_mul_f32_e32 v48, v25, v48
	v_mul_f32_e32 v41, v25, v41
	v_mul_f32_e32 v40, v25, v40
	v_mul_f32_e32 v33, v25, v33
	v_mul_f32_e32 v32, v25, v32
	v_mul_f32_e32 v0, v25, v0
	v_cmp_lt_i32_e32 vcc, v171, v172
	s_waitcnt vmcnt(0)
	v_mul_f32_e32 v6, v6, v81
	v_mul_f32_e32 v7, v7, v80
	v_cvt_pk_bf16_f32 v114, v6, v7
	v_mul_f32_e32 v6, v25, v79
	v_mul_f32_e32 v6, v8, v6
	v_mul_f32_e32 v7, v25, v78
	v_mul_f32_e32 v7, v9, v7
	v_cvt_pk_bf16_f32 v115, v6, v7
	v_mul_f32_e32 v6, v25, v77
	v_mul_f32_e32 v2, v2, v6
	v_mul_f32_e32 v6, v25, v76
	v_mul_f32_e32 v3, v3, v6
	v_cvt_pk_bf16_f32 v116, v2, v3
	v_mul_f32_e32 v2, v25, v75
	v_mul_f32_e32 v3, v25, v74
	v_mul_f32_e32 v2, v4, v2
	v_mul_f32_e32 v3, v5, v3
	v_cvt_pk_bf16_f32 v117, v2, v3
	global_load_dwordx4 v[2:5], v[10:11], off offset:80
	global_load_dwordx4 v[6:9], v[10:11], off offset:64
	s_waitcnt vmcnt(0)
	v_mul_f32_e32 v6, v6, v73
	v_mul_f32_e32 v7, v7, v72
	v_cvt_pk_bf16_f32 v118, v6, v7
	v_mul_f32_e32 v6, v25, v71
	v_mul_f32_e32 v6, v8, v6
	v_mul_f32_e32 v7, v25, v70
	v_mul_f32_e32 v7, v9, v7
	v_cvt_pk_bf16_f32 v119, v6, v7
	v_mul_f32_e32 v6, v25, v69
	v_mul_f32_e32 v2, v6, v2
	v_mul_f32_e32 v6, v25, v68
	v_mul_f32_e32 v3, v6, v3
	v_cvt_pk_bf16_f32 v120, v2, v3
	v_mul_f32_e32 v2, v25, v67
	v_mul_f32_e32 v3, v25, v66
	v_mul_f32_e32 v2, v2, v4
	v_mul_f32_e32 v3, v3, v5
	v_cvt_pk_bf16_f32 v121, v2, v3
	global_load_dwordx4 v[2:5], v[10:11], off offset:144
	global_load_dwordx4 v[6:9], v[10:11], off offset:128
	s_waitcnt vmcnt(0)
	v_mul_f32_e32 v6, v65, v6
	v_mul_f32_e32 v7, v64, v7
	v_cvt_pk_bf16_f32 v122, v6, v7
	v_mul_f32_e32 v6, v25, v63
	v_mul_f32_e32 v6, v6, v8
	v_mul_f32_e32 v7, v25, v62
	v_mul_f32_e32 v7, v7, v9
	v_cvt_pk_bf16_f32 v123, v6, v7
	v_mul_f32_e32 v6, v25, v61
	v_mul_f32_e32 v2, v6, v2
	v_mul_f32_e32 v6, v25, v60
	v_mul_f32_e32 v3, v6, v3
	v_cvt_pk_bf16_f32 v124, v2, v3
	v_mul_f32_e32 v2, v25, v59
	v_mul_f32_e32 v3, v25, v58
	v_mul_f32_e32 v2, v2, v4
	v_mul_f32_e32 v3, v3, v5
	v_cvt_pk_bf16_f32 v125, v2, v3
	global_load_dwordx4 v[2:5], v[10:11], off offset:208
	global_load_dwordx4 v[6:9], v[10:11], off offset:192
	s_waitcnt vmcnt(0)
	v_mul_f32_e32 v6, v57, v6
	v_mul_f32_e32 v7, v56, v7
	v_cvt_pk_bf16_f32 v126, v6, v7
	v_mul_f32_e32 v6, v25, v55
	v_mul_f32_e32 v6, v6, v8
	v_mul_f32_e32 v7, v25, v54
	v_mul_f32_e32 v7, v7, v9
	v_cvt_pk_bf16_f32 v127, v6, v7
	v_mul_f32_e32 v6, v25, v53
	v_mul_f32_e32 v2, v6, v2
	v_mul_f32_e32 v6, v25, v52
	v_mul_f32_e32 v3, v6, v3
	v_cvt_pk_bf16_f32 v128, v2, v3
	v_mul_f32_e32 v2, v25, v51
	v_mul_f32_e32 v3, v25, v50
	v_mul_f32_e32 v2, v2, v4
	v_mul_f32_e32 v3, v3, v5
	v_cvt_pk_bf16_f32 v129, v2, v3
	global_load_dwordx4 v[2:5], v[10:11], off offset:272
	global_load_dwordx4 v[6:9], v[10:11], off offset:256
	s_waitcnt vmcnt(0)
	v_mul_f32_e32 v6, v49, v6
	v_mul_f32_e32 v7, v48, v7
	v_cvt_pk_bf16_f32 v130, v6, v7
	v_mul_f32_e32 v6, v25, v47
	v_mul_f32_e32 v6, v6, v8
	v_mul_f32_e32 v7, v25, v46
	v_mul_f32_e32 v7, v7, v9
	v_cvt_pk_bf16_f32 v131, v6, v7
	v_mul_f32_e32 v6, v25, v45
	v_mul_f32_e32 v2, v6, v2
	v_mul_f32_e32 v6, v25, v44
	v_mul_f32_e32 v3, v6, v3
	v_cvt_pk_bf16_f32 v132, v2, v3
	v_mul_f32_e32 v2, v25, v43
	v_mul_f32_e32 v3, v25, v42
	v_mul_f32_e32 v2, v2, v4
	v_mul_f32_e32 v3, v3, v5
	v_cvt_pk_bf16_f32 v133, v2, v3
	global_load_dwordx4 v[2:5], v[10:11], off offset:336
	global_load_dwordx4 v[6:9], v[10:11], off offset:320
	s_waitcnt vmcnt(0)
	v_mul_f32_e32 v6, v41, v6
	v_mul_f32_e32 v7, v40, v7
	v_cvt_pk_bf16_f32 v134, v6, v7
	v_mul_f32_e32 v6, v25, v39
	v_mul_f32_e32 v6, v6, v8
	v_mul_f32_e32 v7, v25, v38
	v_mul_f32_e32 v7, v7, v9
	v_cvt_pk_bf16_f32 v135, v6, v7
	v_mul_f32_e32 v6, v25, v37
	v_mul_f32_e32 v2, v6, v2
	v_mul_f32_e32 v6, v25, v36
	v_mul_f32_e32 v3, v6, v3
	v_cvt_pk_bf16_f32 v136, v2, v3
	v_mul_f32_e32 v2, v25, v35
	v_mul_f32_e32 v3, v25, v34
	v_mul_f32_e32 v2, v2, v4
	v_mul_f32_e32 v3, v3, v5
	v_cvt_pk_bf16_f32 v137, v2, v3
	global_load_dwordx4 v[2:5], v[10:11], off offset:400
	global_load_dwordx4 v[6:9], v[10:11], off offset:384
	s_waitcnt vmcnt(0)
	v_mul_f32_e32 v6, v33, v6
	v_mul_f32_e32 v7, v32, v7
	v_cvt_pk_bf16_f32 v138, v6, v7
	v_mul_f32_e32 v6, v25, v31
	v_mul_f32_e32 v6, v6, v8
	v_mul_f32_e32 v7, v25, v30
	v_mul_f32_e32 v7, v7, v9
	v_cvt_pk_bf16_f32 v139, v6, v7
	v_mul_f32_e32 v6, v25, v29
	v_mul_f32_e32 v2, v6, v2
	v_mul_f32_e32 v6, v25, v28
	v_mul_f32_e32 v3, v6, v3
	v_cvt_pk_bf16_f32 v140, v2, v3
	v_mul_f32_e32 v2, v25, v27
	v_mul_f32_e32 v3, v25, v26
	v_mul_f32_e32 v2, v2, v4
	v_mul_f32_e32 v3, v3, v5
	v_cvt_pk_bf16_f32 v141, v2, v3
	global_load_dwordx4 v[2:5], v[10:11], off offset:464
	global_load_dwordx4 v[6:9], v[10:11], off offset:448
	v_mul_f32_e32 v10, v25, v24
	v_mov_b32_e32 v11, v1
	s_waitcnt vmcnt(1)
	v_mul_f32_e32 v0, v0, v5
	s_waitcnt vmcnt(0)
	v_mul_f32_e32 v6, v10, v6
	v_mul_f32_e32 v10, v25, v23
	v_mul_f32_e32 v7, v10, v7
	v_cvt_pk_bf16_f32 v142, v6, v7
	v_mul_f32_e32 v6, v25, v22
	v_mul_f32_e32 v6, v6, v8
	v_mul_f32_e32 v7, v25, v21
	v_mul_f32_e32 v7, v7, v9
	v_cvt_pk_bf16_f32 v143, v6, v7
	v_mul_f32_e32 v6, v25, v20
	v_mul_f32_e32 v2, v6, v2
	v_mul_f32_e32 v6, v25, v19
	v_mul_f32_e32 v3, v6, v3
	v_cvt_pk_bf16_f32 v144, v2, v3
	v_mul_f32_e32 v2, v25, v18
	v_ashrrev_i32_e32 v22, 4, v17
	v_mul_f32_e32 v2, v2, v4
	v_cvt_pk_bf16_f32 v145, v2, v0
	v_and_b32_e32 v0, 0xfffff0, v22
	v_lshlrev_b32_e32 v3, 1, v22
	v_lshlrev_b32_e32 v20, 3, v16
	v_and_or_b32 v0, v3, 8, v0
	v_and_b32_e32 v2, 0x78, v20
	v_lshrrev_b32_e32 v3, 1, v22
	v_lshrrev_b32_e32 v0, 1, v0
	v_bfe_u32 v4, v20, 5, 2
	v_and_b32_e32 v5, 3, v22
	v_or_b32_e32 v0, v0, v4
	v_and_or_b32 v3, v3, 4, v5
	v_lshlrev_b32_e32 v23, 1, v2
	v_lshlrev_b32_e32 v0, 9, v0
	v_lshlrev_b32_e32 v3, 6, v3
	v_and_b32_e32 v5, 48, v23
	v_add_u32_e32 v24, 32, v22
	v_or3_b32 v180, v0, v3, v5
	v_and_b32_e32 v0, 0xfffff0, v24
	v_lshlrev_b32_e32 v6, 1, v24
	v_and_or_b32 v0, v6, 8, v0
	v_lshrrev_b32_e32 v0, 1, v0
	v_or_b32_e32 v0, v0, v4
	v_lshlrev_b32_e32 v0, 9, v0
	v_or3_b32 v181, v0, v3, v5
	v_lshl_or_b32 v0, v22, 7, v2
	v_lshlrev_b32_e32 v2, 2, v2
	global_load_dwordx4 v[146:149], v2, s[10:11] offset:16
	global_load_dwordx4 v[150:153], v2, s[10:11]
	global_load_dwordx2 v[4:5], v0, s[8:9]
	v_add_u32_e32 v10, 0x1000, v0
	global_load_dwordx2 v[8:9], v10, s[8:9]
	global_load_dwordx2 v[26:27], v0, s[6:7]
	global_load_dwordx2 v[28:29], v10, s[6:7]
	s_waitcnt vmcnt(0)
	v_lshlrev_b32_e32 v21, 4, v16
	v_lshlrev_b32_e32 v19, 1, v16
	v_and_b32_e32 v18, 0xc0, v21
	v_bitop3_b32 v199, v21, v178, s33 bitop3:0x6c
	s_waitcnt vmcnt(3)
	v_cvt_f32_fp8_e32 v2, v4
	v_cvt_f32_fp8_sdwa v3, v4 src0_sel:BYTE_1
	v_cvt_pk_bf16_f32 v2, v2, v3
	v_cvt_f32_fp8_sdwa v3, v4 src0_sel:BYTE_2
	v_cvt_f32_fp8_sdwa v4, v4 src0_sel:BYTE_3
	v_cvt_pk_bf16_f32 v3, v3, v4
	v_cvt_f32_fp8_e32 v4, v5
	v_cvt_f32_fp8_sdwa v6, v5 src0_sel:BYTE_1
	v_cvt_pk_bf16_f32 v4, v4, v6
	v_cvt_f32_fp8_sdwa v6, v5 src0_sel:BYTE_2
	v_cvt_f32_fp8_sdwa v5, v5 src0_sel:BYTE_3
	v_cvt_pk_bf16_f32 v5, v6, v5
	s_waitcnt vmcnt(2)
	v_cvt_f32_fp8_e32 v6, v8
	v_cvt_f32_fp8_sdwa v7, v8 src0_sel:BYTE_1
	v_cvt_pk_bf16_f32 v6, v6, v7
	v_cvt_f32_fp8_sdwa v7, v8 src0_sel:BYTE_2
	v_cvt_f32_fp8_sdwa v8, v8 src0_sel:BYTE_3
	v_cvt_pk_bf16_f32 v7, v7, v8
	v_cvt_f32_fp8_e32 v8, v9
	v_cvt_f32_fp8_sdwa v25, v9 src0_sel:BYTE_1
	v_cvt_pk_bf16_f32 v8, v8, v25
	v_cvt_f32_fp8_sdwa v25, v9 src0_sel:BYTE_2
	v_cvt_f32_fp8_sdwa v9, v9 src0_sel:BYTE_3
	v_cvt_pk_bf16_f32 v9, v25, v9
	s_waitcnt vmcnt(1)
	v_cvt_f32_fp8_e32 v25, v26
	v_cvt_f32_fp8_sdwa v30, v26 src0_sel:BYTE_1
	v_cvt_pk_bf16_f32 v25, v25, v30
	v_cvt_f32_fp8_sdwa v30, v26 src0_sel:BYTE_2
	v_cvt_f32_fp8_sdwa v26, v26 src0_sel:BYTE_3
	v_cvt_pk_bf16_f32 v26, v30, v26
	v_cvt_f32_fp8_e32 v30, v27
	v_cvt_f32_fp8_sdwa v31, v27 src0_sel:BYTE_1
	v_cvt_pk_bf16_f32 v30, v30, v31
	v_cvt_f32_fp8_sdwa v31, v27 src0_sel:BYTE_2
	v_cvt_f32_fp8_sdwa v27, v27 src0_sel:BYTE_3
	v_cvt_pk_bf16_f32 v27, v31, v27
	s_waitcnt vmcnt(0)
	v_cvt_f32_fp8_e32 v31, v28
	v_cvt_f32_fp8_sdwa v32, v28 src0_sel:BYTE_1
	v_cvt_pk_bf16_f32 v31, v31, v32
	v_cvt_f32_fp8_sdwa v32, v28 src0_sel:BYTE_2
	v_cvt_f32_fp8_sdwa v28, v28 src0_sel:BYTE_3
	v_cvt_pk_bf16_f32 v32, v32, v28
	v_cvt_f32_fp8_e32 v28, v29
	v_cvt_f32_fp8_sdwa v33, v29 src0_sel:BYTE_1
	v_cvt_pk_bf16_f32 v33, v28, v33
	v_cvt_f32_fp8_sdwa v28, v29 src0_sel:BYTE_2
	v_cvt_f32_fp8_sdwa v29, v29 src0_sel:BYTE_3
	v_cvt_pk_bf16_f32 v34, v28, v29
	v_lshlrev_b32_e32 v28, 16, v25
	v_and_b32_e32 v25, 0xffff0000, v25
	v_and_b32_e32 v35, 0xffff0000, v26
	v_lshlrev_b32_e32 v29, 16, v26
	v_lshlrev_b32_e32 v37, 16, v27
	v_and_b32_e32 v38, 0xffff0000, v27
	v_mul_f32_e32 v26, v25, v25
	v_mul_f32_e32 v27, v35, v35
	v_lshlrev_b32_e32 v36, 16, v30
	v_and_b32_e32 v30, 0xffff0000, v30
	v_fmac_f32_e32 v26, v28, v28
	v_fmac_f32_e32 v27, v29, v29
	v_add_f32_e32 v26, v26, v27
	v_mul_f32_e32 v27, v30, v30
	v_fmac_f32_e32 v27, v36, v36
	v_add_f32_e32 v26, v26, v27
	v_mul_f32_e32 v27, v38, v38
	v_fmac_f32_e32 v27, v37, v37
	v_add_f32_e32 v26, v26, v27
	v_cndmask_b32_e32 v27, v170, v171, vcc
	v_lshlrev_b32_e32 v185, 2, v27
	s_nop 1
	v_cmp_lt_i32_e32 vcc, v173, v172
	v_add_f32_dpp v26, v26, v26 quad_perm:[1,0,3,2] row_mask:0xf bank_mask:0xf
	v_cndmask_b32_e32 v27, v170, v173, vcc
	v_lshlrev_b32_e32 v186, 2, v27
	s_nop 1
	v_cmp_lt_i32_e32 vcc, v174, v172
	v_add_f32_dpp v26, v26, v26 quad_perm:[2,3,0,1] row_mask:0xf bank_mask:0xf
	v_cndmask_b32_e32 v27, v170, v174, vcc
	v_lshlrev_b32_e32 v187, 2, v27
	s_nop 1
	v_cmp_lt_i32_e32 vcc, v175, v172
	v_add_f32_dpp v26, v26, v26 row_half_mirror row_mask:0xf bank_mask:0xf
	v_cndmask_b32_e32 v27, v170, v175, vcc
	v_lshlrev_b32_e32 v188, 2, v27
	s_nop 1
	s_waitcnt lgkmcnt(0)
	v_add_f32_dpp v26, v26, v26 row_mirror row_mask:0xf bank_mask:0xf
	v_fmamk_f32 v26, v26, 0x3c000000, v167
	v_rsq_f32_e32 v39, v26
	s_nop 0
	v_mul_f32_e32 v26, v39, v28
	v_mul_f32_e32 v25, v39, v25
	v_mul_f32_e32 v26, v150, v26
	v_mul_f32_e32 v25, v151, v25
	v_cvt_pk_bf16_f32 v26, v26, v25
	v_mul_f32_e32 v25, v39, v29
	v_mul_f32_e32 v27, v39, v35
	v_mul_f32_e32 v25, v152, v25
	v_mul_f32_e32 v27, v153, v27
	v_cvt_pk_bf16_f32 v27, v25, v27
	v_mul_f32_e32 v25, v39, v36
	v_mul_f32_e32 v28, v39, v30
	v_mul_f32_e32 v25, v146, v25
	v_mul_f32_e32 v28, v147, v28
	v_cvt_pk_bf16_f32 v28, v25, v28
	v_mul_f32_e32 v25, v39, v37
	v_mul_f32_e32 v29, v39, v38
	v_mul_f32_e32 v25, v148, v25
	v_mul_f32_e32 v29, v149, v29
	v_cvt_pk_bf16_f32 v29, v25, v29
	v_lshlrev_b32_e32 v25, 16, v31
	v_and_b32_e32 v30, 0xffff0000, v31
	v_lshlrev_b32_e32 v31, 16, v32
	v_and_b32_e32 v32, 0xffff0000, v32
	v_mul_f32_e32 v37, v30, v30
	v_mul_f32_e32 v38, v32, v32
	v_lshlrev_b32_e32 v35, 16, v33
	v_and_b32_e32 v33, 0xffff0000, v33
	v_fmac_f32_e32 v37, v25, v25
	v_fmac_f32_e32 v38, v31, v31
	v_add_f32_e32 v37, v37, v38
	v_mul_f32_e32 v38, v33, v33
	v_lshlrev_b32_e32 v36, 16, v34
	v_and_b32_e32 v34, 0xffff0000, v34
	v_fmac_f32_e32 v38, v35, v35
	v_add_f32_e32 v37, v37, v38
	v_mul_f32_e32 v38, v34, v34
	v_fmac_f32_e32 v38, v36, v36
	v_add_f32_e32 v37, v37, v38
	s_nop 1
	v_add_f32_dpp v37, v37, v37 quad_perm:[1,0,3,2] row_mask:0xf bank_mask:0xf
	s_nop 1
	v_add_f32_dpp v37, v37, v37 quad_perm:[2,3,0,1] row_mask:0xf bank_mask:0xf
	s_nop 1
	v_add_f32_dpp v37, v37, v37 row_half_mirror row_mask:0xf bank_mask:0xf
	s_nop 1
	s_waitcnt lgkmcnt(0)
	v_add_f32_dpp v37, v37, v37 row_mirror row_mask:0xf bank_mask:0xf
	v_fmamk_f32 v37, v37, 0x3c000000, v167
	v_rsq_f32_e32 v37, v37
	s_nop 0
	v_cmp_gt_u32_e64 s[4:5], 32, v16
	v_mul_f32_e32 v25, v37, v25
	v_mul_f32_e32 v30, v37, v30
	v_mul_f32_e32 v25, v150, v25
	v_mul_f32_e32 v30, v151, v30
	v_cvt_pk_bf16_f32 v30, v25, v30
	v_mul_f32_e32 v25, v37, v31
	v_mul_f32_e32 v31, v37, v32
	v_mul_f32_e32 v25, v152, v25
	v_mul_f32_e32 v31, v153, v31
	v_cvt_pk_bf16_f32 v31, v25, v31
	v_mul_f32_e32 v25, v37, v35
	v_mul_f32_e32 v32, v37, v33
	v_mul_f32_e32 v25, v146, v25
	v_mul_f32_e32 v32, v147, v32
	v_cvt_pk_bf16_f32 v32, v25, v32
	v_mul_f32_e32 v25, v37, v36
	v_mul_f32_e32 v33, v37, v34
	v_mul_f32_e32 v25, v148, v25
	v_mul_f32_e32 v33, v149, v33
	v_cvt_pk_bf16_f32 v33, v25, v33
	v_add_u32_e32 v25, 0, v180
	ds_write_b128 v25, v[2:5]
	v_add_u32_e32 v2, 0, v181
	ds_write_b128 v2, v[6:9]
	v_lshlrev_b32_e32 v2, 8, v22
	v_and_b32_e32 v3, 0xf0, v17
	v_bitop3_b32 v196, v23, v2, v3 bitop3:0xde
	v_add_u32_e32 v2, 0, v196
	ds_write_b128 v2, v[26:29] offset:32768
	v_lshlrev_b32_e32 v2, 8, v24
	v_bitop3_b32 v198, v2, v23, v3 bitop3:0xf6
	v_med3_i32 v3, s85, 4, v169
	v_add_u32_e32 v2, 0, v198
	v_readfirstlane_b32 s88, v3
	v_ashrrev_i32_e32 v3, 3, v13
	v_and_b32_e32 v4, -4, v3
	v_sub_u32_e32 v5, v4, v14
	v_cmp_gt_u32_e64 s[70:71], 16, v5
	v_sub_u32_e32 v5, v4, v15
	v_add_u32_e32 v6, 40, v5
	v_cmp_gt_u32_e64 s[68:69], 16, v6
	v_add_u32_e32 v6, 9, v5
	v_cmp_gt_u32_e64 s[66:67], 16, v6
	v_add_u32_e32 v6, 41, v5
	v_cmp_gt_u32_e64 s[64:65], 16, v6
	v_add_u32_e32 v6, 10, v5
	ds_write_b128 v2, v[30:33] offset:32768
	v_add_u32_e32 v2, 32, v178
	v_cmp_gt_u32_e64 s[62:63], 16, v6
	v_add_u32_e32 v6, 42, v5
	v_bitop3_b32 v197, v2, v21, s33 bitop3:0x78
	v_add_u32_e32 v2, 64, v178
	v_cmp_gt_u32_e64 s[60:61], 16, v6
	v_add_u32_e32 v6, 17, v5
	v_bitop3_b32 v195, v2, v21, s33 bitop3:0x78
	v_add_u32_e32 v2, 0x60, v178
	v_or_b32_e32 v3, 3, v3
	v_cmp_gt_u32_e64 s[50:51], 16, v6
	v_add_u32_e32 v6, 49, v5
	v_bitop3_b32 v194, v2, v21, s33 bitop3:0x78
	v_add_u32_e32 v2, 0x80, v178
	v_sub_u32_e32 v3, v3, v14
	v_cmp_gt_u32_e64 s[48:49], 16, v6
	v_add_u32_e32 v6, 18, v5
	v_bitop3_b32 v193, v2, v21, s33 bitop3:0x78
	v_add_u32_e32 v2, 0xa0, v178
	v_cmp_gt_u32_e64 s[58:59], 16, v3
	v_add_u32_e32 v3, 43, v5
	v_cmp_gt_u32_e64 s[46:47], 16, v6
	v_add_u32_e32 v6, 50, v5
	v_bitop3_b32 v192, v2, v21, s33 bitop3:0x78
	v_add_u32_e32 v2, 0xc0, v178
	v_cmp_gt_u32_e64 s[56:57], 16, v3
	v_cmp_lt_u32_e64 s[54:55], s1, v5
	v_and_b32_e32 v3, -16, v5
	s_movk_i32 s1, 0xffd0
	v_cmp_gt_u32_e64 s[44:45], 16, v6
	v_add_u32_e32 v6, 19, v5
	v_bitop3_b32 v191, v2, v21, s33 bitop3:0x78
	v_add_u32_e32 v2, 0xe0, v178
	s_add_i32 s84, s88, -4
	s_add_i32 s88, s88, 4
	v_cmp_eq_u32_e64 s[52:53], s1, v3
	v_cmp_gt_u32_e64 s[42:43], 16, v6
	v_add_u32_e32 v6, 51, v5
	s_movk_i32 s1, 0xffe0
	v_bitop3_b32 v190, v2, v21, s33 bitop3:0x78
	v_and_b32_e32 v2, 0x118, v20
	v_cmp_gt_u32_e64 s[40:41], 16, v6
	v_add_u32_e32 v6, 24, v5
	v_cmp_eq_u32_e64 s[20:21], s1, v3
	s_movk_i32 s1, 0xffc0
	s_cmp_lg_u32 0, -1
	v_and_or_b32 v2, v19, 32, v2
	v_cmp_gt_u32_e64 s[38:39], 16, v6
	v_add_u32_e32 v6, 56, v5
	v_cmp_eq_u32_e64 s[18:19], s1, v3
	s_cselect_b32 s1, 0, 0
	v_cmp_gt_u32_e64 s[36:37], 16, v6
	v_add_u32_e32 v6, 25, v5
	v_add_u32_e32 v3, 33, v5
	v_add3_u32 v182, v18, s1, v2
	v_readlane_b32 s1, v252, 25
	v_cmp_gt_u32_e64 s[34:35], 16, v6
	v_add_u32_e32 v6, 57, v5
	v_cmp_gt_u32_e64 s[16:17], 16, v3
	v_add_u32_e32 v3, 0x41, v5
	s_sub_i32 s2, s1, s86
	v_cmp_gt_u32_e64 s[30:31], 16, v6
	v_add_u32_e32 v6, 26, v5
	v_cmp_gt_u32_e64 s[14:15], 16, v3
	v_add_u32_e32 v3, 34, v5
	s_add_u32 s1, s78, s96
	v_cmp_gt_u32_e64 s[28:29], 16, v6
	v_add_u32_e32 v6, 58, v5
	v_cmp_gt_u32_e64 s[12:13], 16, v3
	v_add_u32_e32 v3, 0x42, v5
	s_addc_u32 s86, s79, s97
	v_cmp_gt_u32_e64 s[26:27], 16, v6
	v_add_u32_e32 v6, 27, v5
	v_cmp_gt_u32_e64 s[10:11], 16, v3
	v_add_u32_e32 v3, 35, v5
	s_add_u32 s72, s1, s72
	v_cmp_gt_u32_e64 s[24:25], 16, v6
	v_add_u32_e32 v6, 59, v5
	v_cmp_gt_u32_e64 s[8:9], 16, v3
	v_add_u32_e32 v3, 0x43, v5
	s_addc_u32 s73, s86, s73
	v_mov_b32_e32 v14, v1
	v_mov_b32_e32 v15, v1
	v_cmp_gt_u32_e64 s[22:23], 16, v6
	v_cmp_gt_u32_e64 s[6:7], 16, v3
	v_sub_u32_e32 v183, v4, v12
	v_lshl_add_u64 v[154:155], s[72:73], 0, v[0:1]
	v_lshl_add_u64 v[156:157], s[72:73], 0, v[10:11]
	v_mov_b32_e32 v0, v1
	v_mov_b32_e32 v2, v1
	v_mov_b32_e32 v3, v1
	v_mov_b32_e32 v4, v1
	v_mov_b32_e32 v5, v1
	v_mov_b32_e32 v6, v1
	v_mov_b32_e32 v7, v1
	v_mov_b32_e32 v8, v1
	v_mov_b32_e32 v9, v1
	v_mov_b32_e32 v10, v1
	v_mov_b32_e32 v12, v1
	v_mov_b32_e32 v13, v1
	v_mov_b64_e32 v[64:65], v[14:15]
	v_mov_b64_e32 v[48:49], v[14:15]
	v_mov_b64_e32 v[32:33], v[14:15]
	v_mov_b64_e32 v[62:63], v[12:13]
	v_mov_b64_e32 v[60:61], v[10:11]
	v_mov_b64_e32 v[58:59], v[8:9]
	v_mov_b64_e32 v[56:57], v[6:7]
	v_mov_b64_e32 v[54:55], v[4:5]
	v_mov_b64_e32 v[52:53], v[2:3]
	v_mov_b64_e32 v[50:51], v[0:1]
	v_mov_b64_e32 v[46:47], v[12:13]
	v_mov_b64_e32 v[44:45], v[10:11]
	v_mov_b64_e32 v[42:43], v[8:9]
	v_mov_b64_e32 v[40:41], v[6:7]
	v_mov_b64_e32 v[38:39], v[4:5]
	v_mov_b64_e32 v[36:37], v[2:3]
	v_mov_b64_e32 v[34:35], v[0:1]
	v_mov_b64_e32 v[30:31], v[12:13]
	v_mov_b64_e32 v[28:29], v[10:11]
	v_mov_b64_e32 v[26:27], v[8:9]
	v_mov_b64_e32 v[24:25], v[6:7]
	v_mov_b64_e32 v[22:23], v[4:5]
	v_mov_b64_e32 v[20:21], v[2:3]
	v_mov_b64_e32 v[18:19], v[0:1]
	v_mov_b64_e32 v[16:17], v[14:15]
	s_mov_b64 s[96:97], 0
	v_mov_b64_e32 v[14:15], v[12:13]
	v_mov_b64_e32 v[12:13], v[10:11]
	v_mov_b64_e32 v[10:11], v[8:9]
	v_mov_b64_e32 v[8:9], v[6:7]
	v_mov_b64_e32 v[6:7], v[4:5]
	v_mov_b64_e32 v[4:5], v[2:3]
	v_mov_b64_e32 v[2:3], v[0:1]
	s_waitcnt lgkmcnt(0)
	s_barrier
